# prologue: 1 static conversion round and 6656 items through the work counter
# baseline (speedup 1.0000x reference)
.LBB0_41:
	v_writelane_b32 v253, s24, 32
	v_writelane_b32 v253, s23, 34
	v_writelane_b32 v253, s22, 36
	s_mov_b32 s3, 0
	v_readlane_b32 s0, v253, 29
	s_lshl_b32 s0, s0, 14
	s_add_i32 s29, s0, 0
	s_cmp_lg_u64 s[48:49], 0
	v_readlane_b32 s4, v253, 30
	s_cselect_b64 s[44:45], -1, 0
	s_abs_i32 s2, s4
	v_cvt_f32_u32_e32 v2, s2
	s_sub_i32 s0, 0, s2
	s_ashr_i32 s6, s4, 31
	v_rcp_iflag_f32_e32 v2, v2
	s_nop 0
	v_mul_f32_e32 v2, 0x4f7ffffe, v2
	v_cvt_u32_f32_e32 v2, v2
	s_nop 0
	v_readfirstlane_b32 s1, v2
	s_mul_i32 s0, s0, s1
	s_mul_hi_u32 s0, s1, s0
	s_add_i32 s7, s1, s0
	s_mul_hi_u32 s0, s7, 0x4200
	s_mul_i32 s0, s0, s2
	s_sub_i32 s0, 0x4200, s0
	s_sub_i32 s1, s0, s2
	s_cmp_ge_u32 s0, s2
	s_cselect_b32 s0, s1, s0
	s_sub_i32 s1, s0, s2
	s_cmp_ge_u32 s0, s2
	s_cselect_b32 s8, s1, s0
	s_add_i32 s0, s4, 0xffffff00
	s_cmp_ge_i32 s0, s8
	s_cselect_b64 s[0:1], -1, 0
	s_cmpk_lt_u32 s8, 0x2101
	s_cselect_b64 s[4:5], -1, 0
	s_sub_i32 s8, 0x4200, s8
	s_and_b64 s[0:1], s[0:1], s[4:5]
	s_and_b64 s[0:1], s[0:1], exec
	s_cselect_b32 s5, s8, 0x4200
	s_add_i32 s0, s5, 0xffffe200
	s_cmp_eq_u32 s2, 0x800
	s_cselect_b32 s5, s0, s5
	v_writelane_b32 v253, s5, 38
	v_writelane_b32 v253, s48, 40
	s_mul_hi_u32 s0, s5, s7
	s_mul_i32 s1, s0, s2
	v_writelane_b32 v253, s49, 41
	v_writelane_b32 v253, s50, 42
	v_writelane_b32 v253, s51, 43
	v_writelane_b32 v253, s52, 44
	v_writelane_b32 v253, s53, 45
	v_writelane_b32 v253, s54, 46
	v_writelane_b32 v253, s55, 47
	s_sub_i32 s1, s5, s1
	v_writelane_b32 v253, s56, 48
	s_add_i32 s4, s0, 1
	s_sub_i32 s5, s1, s2
	v_writelane_b32 v253, s57, 49
	s_cmp_ge_u32 s1, s2
	v_writelane_b32 v253, s58, 50
	s_cselect_b32 s0, s4, s0
	v_writelane_b32 v253, s59, 51
	s_cselect_b32 s1, s5, s1
	s_add_i32 s4, s0, 1
	v_writelane_b32 v253, s60, 52
	s_cmp_ge_u32 s1, s2
	v_writelane_b32 v253, s61, 53
	s_cselect_b32 s0, s4, s0
	v_writelane_b32 v253, s62, 54
	s_xor_b32 s0, s0, s6
	v_writelane_b32 v253, s63, 55
	s_sub_i32 s15, s0, s6
	v_writelane_b32 v253, s29, 56
	s_add_i32 s14, s15, -3
	v_writelane_b32 v253, s44, 57
	s_cmp_lt_i32 s15, 1
	v_readfirstlane_b32 s0, v0
	v_writelane_b32 v253, s45, 58
	s_cbranch_scc1 .LBB0_65
	s_ashr_i32 s0, s0, 8
	s_min_i32 s18, s0, s14
	s_cmpk_gt_i32 s27, 0x7ff
	v_readlane_b32 s0, v253, 26
	s_cselect_b64 s[20:21], -1, 0
	s_add_u32 s0, s0, 0x800000
	v_writelane_b32 v253, s0, 59
	v_mov_b32_e32 v133, 0
	v_readlane_b32 s0, v253, 27
	s_addc_u32 s0, s0, 0
	s_add_i32 s25, 0, 0x21000
	v_writelane_b32 v253, s0, 61
	s_add_i32 s0, 0, 0x21200
	v_writelane_b32 v253, s0, 63
	s_add_i32 s0, 0, 0x21100
	v_writelane_b32 v254, s0, 1
	s_add_i32 s0, 0, 0x21300
	v_writelane_b32 v254, s0, 3
	v_writelane_b32 v254, s27, 5
	v_writelane_b32 v254, s14, 7
	v_writelane_b32 v254, s15, 9
	v_writelane_b32 v254, s18, 11
	v_writelane_b32 v254, s20, 13
	s_mov_b32 s22, 0x42800000
	s_mov_b32 s19, 0
	v_writelane_b32 v254, s21, 14
	s_branch .LBB0_45
